# weight conversion shares: 1360 more gate tiles converted ahead by the down-GEMM filler (phase-1 loop 6.5 tiles per wave)
# speedup vs baseline: 1.0016x; 1.0016x over previous
.LBB0_78:
	s_or_b64 exec, exec, s[0:1]
	v_readlane_b32 s0, v255, 6
	v_readlane_b32 s1, v255, 7
	s_mov_b32 s21, s1
	v_readlane_b32 s0, v251, 1
	s_lshl_b64 s[16:17], s[20:21], 12
	v_readlane_b32 s8, v251, 9
	v_readlane_b32 s10, v251, 11
	v_readlane_b32 s11, v251, 12
	v_readlane_b32 s12, v251, 13
	v_readlane_b32 s9, v251, 10
	v_readlane_b32 s13, v251, 14
	s_add_u32 s8, s12, s16
	v_sub_co_u32_e64 v2, s[10:11], s20, 1
	v_writelane_b32 v255, s16, 28
	s_addc_u32 s9, s13, s17
	s_xor_b64 s[12:13], s[10:11], -1
	v_readlane_b32 s1, v251, 2
	v_readlane_b32 s14, v251, 15
	v_readlane_b32 s15, v251, 16
	s_cmp_lg_u32 s20, 0
	s_cselect_b64 s[14:15], -1, 0
	s_and_b64 s[0:1], s[10:11], exec
	v_readlane_b32 s2, v251, 3
	s_cselect_b32 s0, 0, 0x3550
	v_writelane_b32 v255, s17, 29
	s_add_i32 s2, s0, s89
	s_lshl_b64 s[16:17], s[20:21], 27
	s_lshl_b64 s[0:1], s[20:21], 22
	v_readlane_b32 s3, v251, 4
	s_add_u32 s18, s68, s16
	s_addc_u32 s19, s69, s17
	v_readlane_b32 s3, v251, 57
	s_add_u32 s78, s3, s26
	v_readlane_b32 s3, v251, 58
	v_readlane_b32 s4, v251, 5
	s_addc_u32 s79, s3, 0
	v_readlane_b32 s3, v251, 59
	v_readlane_b32 s5, v251, 6
	s_add_u32 s4, s3, s26
	v_readlane_b32 s3, v251, 60
	s_addc_u32 s5, s3, 0
	v_readlane_b32 s36, v251, 35
	v_writelane_b32 v255, s4, 30
	v_readlane_b32 s48, v251, 47
	v_readlane_b32 s49, v251, 48
	v_writelane_b32 v255, s5, 31
	s_mov_b64 s[4:5], s[20:21]
	s_add_u32 s20, s48, s0
	v_mov_b32_e32 v3, v0
	s_addc_u32 s21, s49, s1
	v_readlane_b32 s0, v251, 61
	v_ashrrev_i32_e32 v4, 6, v3
	v_add_u32_e32 v117, s2, v4
	s_add_u32 s2, s0, s26
	v_readlane_b32 s0, v251, 62
	s_addc_u32 s3, s0, 0
	v_readlane_b32 s0, v251, 63
	v_readlane_b32 s37, v251, 36
	v_readlane_b32 s38, v251, 37
	v_readlane_b32 s39, v251, 38
	v_readlane_b32 s40, v251, 39
	v_readlane_b32 s41, v251, 40
	v_readlane_b32 s42, v251, 41
	v_readlane_b32 s43, v251, 42
	v_readlane_b32 s44, v251, 43
	v_readlane_b32 s45, v251, 44
	v_readlane_b32 s46, v251, 45
	v_readlane_b32 s47, v251, 46
	v_readlane_b32 s50, v251, 49
	v_readlane_b32 s51, v251, 50
	s_add_u32 s34, s0, s26
	v_readlane_b32 s0, v252, 0
	s_addc_u32 s35, s0, 0
	s_mul_i32 s1, s4, 0x1b10000
	v_readlane_b32 s36, v251, 19
	s_mul_hi_u32 s0, s4, 0x1b10000
	v_readlane_b32 s37, v251, 20
	s_add_u32 s22, s36, s1
	v_readlane_b32 s38, v251, 21
	v_readlane_b32 s39, v251, 22
	s_addc_u32 s23, s37, s0
	s_movk_i32 s0, 0x4100
	v_lshlrev_b32_e32 v5, 2, v3
	s_mul_hi_u32 s39, s4, 9
	s_mul_i32 s38, s4, 9
	v_mul_hi_u32 v115, v2, 9
	v_mul_lo_u32 v114, v2, 9
	v_mul_lo_u32 v2, v4, s0
	v_bfe_u32 v123, v3, 4, 2
	v_and_b32_e32 v162, 60, v5
	v_bfe_u32 v164, v3, 3, 3
	v_lshlrev_b32_e32 v3, 3, v3
	s_mul_hi_u32 s25, s4, 3
	v_writelane_b32 v255, s4, 32
	v_add_u32_e32 v2, 0, v2
	v_lshlrev_b32_e32 v5, 2, v162
	v_mul_u32_u24_e32 v6, 0x104, v123
	v_and_b32_e32 v116, 56, v3
	v_writelane_b32 v255, s5, 33
	v_readlane_b32 s0, v252, 1
	v_add3_u32 v163, v2, v5, v6
	v_mul_u32_u24_e32 v3, 0x104, v116
	v_lshlrev_b32_e32 v5, 2, v164
	v_writelane_b32 v255, s2, 34
	s_add_u32 s30, s0, s26
	v_readlane_b32 s0, v252, 2
	v_add3_u32 v165, v2, v3, v5
	v_lshlrev_b32_e32 v130, 1, v116
	v_writelane_b32 v255, s3, 35
	s_addc_u32 s31, s0, 0
	v_mov_b32_e32 v2, 0xffff6d60
	s_movk_i32 s0, 0x6950
	s_mul_i32 s24, s4, 3
	v_lshl_add_u64 v[118:119], s[2:3], 0, v[130:131]
	v_writelane_b32 v255, s26, 36
	v_lshl_add_u64 v[120:121], s[30:31], 0, v[130:131]
	v_mul_u32_u24_e32 v122, 0x1b10, v123
	v_lshl_add_u32 v166, v117, 1, v2
	v_lshl_add_u32 v167, v117, 14, v241
	v_lshl_add_u32 v168, v117, 3, v250
	v_cmp_gt_i32_e64 s[2:3], s0, v117
	v_cmp_gt_i32_e64 s[26:27], 4, v4
	v_cmp_lt_i32_e64 s[0:1], 3, v4
	s_mov_b64 s[28:29], -1
	v_readlane_b32 s6, v251, 7
	v_readlane_b32 s7, v251, 8
	v_readlane_b32 s40, v251, 23
	v_readlane_b32 s41, v251, 24
	v_readlane_b32 s42, v251, 25
	v_readlane_b32 s43, v251, 26
	v_readlane_b32 s44, v251, 27
	v_readlane_b32 s45, v251, 28
	v_readlane_b32 s46, v251, 29
	v_readlane_b32 s47, v251, 30
	v_readlane_b32 s48, v251, 31
	v_readlane_b32 s49, v251, 32
	v_readlane_b32 s50, v251, 33
	v_readlane_b32 s51, v251, 34
	s_branch .LBB0_80

.LBB0_1014:
	v_readlane_b32 s0, v253, 17
	v_readlane_b32 s1, v253, 18
	s_andn2_b64 vcc, exec, s[0:1]
	s_cbranch_vccnz .LBB0_1047
	v_mov_b32_e32 v2, v0
	v_readlane_b32 s0, v253, 19
	v_ashrrev_i32_e32 v4, 6, v2
	s_nop 0
	v_add_u32_e32 v3, s0, v4
	v_cmp_gt_i32_e32 vcc, s44, v3
	s_and_saveexec_b64 s[2:3], vcc
	s_cbranch_execz .LBB0_1046
	s_movk_i32 s0, 0x4100
	v_readlane_b32 s8, v255, 41
	v_mul_lo_u32 v4, v4, s0
	v_readlane_b32 s0, v255, 6
	s_mov_b32 s10, s8
	v_readlane_b32 s1, v255, 7
	v_readlane_b32 s9, v255, 42
	v_writelane_b32 v255, s10, 41
	s_mov_b32 s9, s1
	s_lshl_b64 s[4:5], s[8:9], 27
	v_writelane_b32 v255, s11, 42
	s_lshl_b64 s[0:1], s[8:9], 22
	s_mul_hi_u32 s7, s8, 3
	s_mul_i32 s6, s8, 3
	s_mul_hi_u32 s15, s8, 0x1b10000
	s_mul_i32 s14, s8, 0x1b10000
	v_readlane_b32 s8, v251, 59
	v_readlane_b32 s16, v255, 43
	s_add_u32 s8, s8, s16
	v_readlane_b32 s9, v251, 60
	v_readlane_b32 s40, v251, 35
	s_addc_u32 s9, s9, 0
	v_readlane_b32 s52, v251, 47
	v_lshlrev_b32_e32 v5, 2, v2
	v_readlane_b32 s53, v251, 48
	s_add_u32 s10, s52, s0
	v_bfe_u32 v9, v2, 4, 2
	v_and_b32_e32 v48, 60, v5
	v_bfe_u32 v50, v2, 3, 3
	v_lshlrev_b32_e32 v2, 3, v2
	s_addc_u32 s11, s53, s1
	v_readlane_b32 s0, v251, 61
	v_add_u32_e32 v4, 0, v4
	v_lshlrev_b32_e32 v5, 2, v48
	v_mul_u32_u24_e32 v6, 0x104, v9
	v_and_b32_e32 v2, 56, v2
	s_add_u32 s0, s0, s16
	v_readlane_b32 s1, v251, 62
	v_add3_u32 v49, v4, v5, v6
	v_mul_u32_u24_e32 v5, 0x104, v2
	v_lshlrev_b32_e32 v6, 2, v50
	s_addc_u32 s1, s1, 0
	v_lshlrev_b32_e32 v130, 1, v2
	v_add3_u32 v51, v4, v5, v6
	v_lshl_add_u64 v[4:5], s[0:1], 0, v[130:131]
	v_readlane_b32 s0, v251, 63
	v_readlane_b32 s41, v251, 36
	v_readlane_b32 s42, v251, 37
	v_readlane_b32 s43, v251, 38
	v_readlane_b32 s44, v251, 39
	v_readlane_b32 s45, v251, 40
	v_readlane_b32 s46, v251, 41
	v_readlane_b32 s47, v251, 42
	v_readlane_b32 s48, v251, 43
	v_readlane_b32 s49, v251, 44
	v_readlane_b32 s50, v251, 45
	v_readlane_b32 s51, v251, 46
	v_readlane_b32 s54, v251, 49
	v_readlane_b32 s55, v251, 50
	s_add_u32 s12, s0, s16
	v_readlane_b32 s0, v252, 0
	s_addc_u32 s13, s0, 0
	v_readlane_b32 s40, v251, 19
	v_readlane_b32 s41, v251, 20
	s_add_u32 s14, s40, s14
	s_addc_u32 s15, s41, s15
	v_readlane_b32 s0, v252, 1
	s_add_u32 s0, s0, s16
	v_readlane_b32 s1, v252, 2
	s_addc_u32 s1, s1, 0
	v_add_u32_e32 v3, 0x2950, v3
	v_lshl_add_u64 v[6:7], s[0:1], 0, v[130:131]
	s_mov_b32 s0, 0x6c400
	v_readlane_b32 s54, v251, 33
	v_mul_lo_u32 v8, v3, s0
	s_movk_i32 s54, 0x1000
	v_mad_u32_u24 v8, v9, s33, v8
	v_lshlrev_b32_e32 v52, 6, v3
	v_lshlrev_b32_e32 v53, 2, v3
	v_lshl_add_u32 v54, v3, 14, v241
	v_lshl_add_u32 v55, v3, 3, v250
	s_mov_b64 s[16:17], 0
	v_readlane_b32 s42, v251, 21
	v_readlane_b32 s43, v251, 22
	v_readlane_b32 s44, v251, 23
	v_readlane_b32 s45, v251, 24
	v_readlane_b32 s46, v251, 25
	v_readlane_b32 s47, v251, 26
	v_readlane_b32 s48, v251, 27
	v_readlane_b32 s49, v251, 28
	v_readlane_b32 s50, v251, 29
	v_readlane_b32 s51, v251, 30
	v_readlane_b32 s52, v251, 31
	v_readlane_b32 s53, v251, 32
	v_readlane_b32 s55, v251, 34
	s_branch .LBB0_1019

.LBB0_1018:
	s_or_b64 exec, exec, s[18:19]
	s_movk_i32 s0, 0x334f
	v_add_u32_e32 v10, 0x200, v3
	v_cmp_lt_i32_e32 vcc, s0, v3
	v_add_u32_e32 v8, 0xd880000, v8
	v_add_u32_e32 v52, 0x8000, v52
	v_add_u32_e32 v53, 0x800, v53
	v_add_u32_e32 v54, 0x800000, v54
	v_add_u32_e32 v55, 0x1000, v55
	s_or_b64 s[16:17], vcc, s[16:17]
	v_mov_b32_e32 v3, v10
	s_andn2_b64 exec, exec, s[16:17]
	s_cbranch_execz .LBB0_1046

.LBB0_1404:
	v_readlane_b32 s0, v254, 10
	v_readlane_b32 s2, v255, 37
	v_readlane_b32 s1, v254, 11
	v_readlane_b32 s3, v255, 38
	s_or_b64 s[0:1], s[0:1], s[2:3]
	s_and_b64 vcc, exec, s[0:1]
	s_cbranch_vccnz .LBB0_1437
	v_mov_b32_e32 v2, v0
	v_readlane_b32 s0, v254, 12
	v_ashrrev_i32_e32 v4, 6, v2
	s_nop 0
	v_add_u32_e32 v3, s0, v4
	s_movk_i32 s0, 0x2950
	v_cmp_gt_i32_e32 vcc, s0, v3
	s_and_saveexec_b64 s[2:3], vcc
	s_cbranch_execz .LBB0_1436
	v_readlane_b32 s0, v255, 6
	v_readlane_b32 s6, v255, 41
	v_readlane_b32 s1, v255, 7
	v_readlane_b32 s7, v255, 42
	s_mov_b32 s7, s1
	s_mov_b32 s8, s6
	s_lshl_b64 s[0:1], s[6:7], 27
	s_lshl_b64 s[10:11], s[6:7], 22
	v_writelane_b32 v255, s8, 41
	s_mul_hi_u32 s5, s6, 3
	s_mul_i32 s4, s6, 3
	s_mul_hi_u32 s15, s6, 0x1b10000
	v_writelane_b32 v255, s9, 42
	s_mul_i32 s14, s6, 0x1b10000
	s_add_u32 s6, s64, s0
	s_addc_u32 s7, s65, s1
	v_readlane_b32 s0, v251, 59
	v_readlane_b32 s34, v255, 43
	s_add_u32 s8, s0, s34
	v_readlane_b32 s0, v251, 60
	v_readlane_b32 s16, v251, 35
	s_addc_u32 s9, s0, 0
	v_readlane_b32 s28, v251, 47
	v_readlane_b32 s29, v251, 48
	s_add_u32 s10, s28, s10
	v_readlane_b32 s17, v251, 36
	v_readlane_b32 s18, v251, 37
	v_readlane_b32 s19, v251, 38
	v_readlane_b32 s20, v251, 39
	v_readlane_b32 s21, v251, 40
	v_readlane_b32 s22, v251, 41
	v_readlane_b32 s23, v251, 42
	v_readlane_b32 s24, v251, 43
	v_readlane_b32 s25, v251, 44
	v_readlane_b32 s26, v251, 45
	v_readlane_b32 s27, v251, 46
	v_readlane_b32 s30, v251, 49
	v_readlane_b32 s31, v251, 50
	s_addc_u32 s11, s29, s11
	v_readlane_b32 s0, v251, 61
	s_add_u32 s0, s0, s34
	v_readlane_b32 s1, v251, 62
	v_readlane_b32 s16, v251, 19
	s_addc_u32 s1, s1, 0
	v_readlane_b32 s12, v251, 63
	v_readlane_b32 s18, v251, 21
	s_add_u32 s12, s12, s34
	v_readlane_b32 s13, v252, 0
	s_movk_i32 s18, 0x4100
	v_lshlrev_b32_e32 v5, 2, v2
	s_addc_u32 s13, s13, 0
	v_mul_lo_u32 v4, v4, s18
	v_bfe_u32 v9, v2, 4, 2
	v_and_b32_e32 v48, 60, v5
	v_bfe_u32 v50, v2, 3, 3
	v_lshlrev_b32_e32 v2, 3, v2
	v_readlane_b32 s17, v251, 20
	s_add_u32 s14, s16, s14
	v_add_u32_e32 v4, 0, v4
	v_lshlrev_b32_e32 v5, 2, v48
	v_mul_u32_u24_e32 v6, 0x104, v9
	v_and_b32_e32 v2, 56, v2
	s_addc_u32 s15, s17, s15
	v_readlane_b32 s16, v252, 1
	v_add3_u32 v49, v4, v5, v6
	v_mul_u32_u24_e32 v5, 0x104, v2
	v_lshlrev_b32_e32 v6, 2, v50
	v_lshlrev_b32_e32 v130, 1, v2
	s_add_u32 s16, s16, s34
	v_readlane_b32 s17, v252, 2
	v_add3_u32 v51, v4, v5, v6
	v_lshl_add_u64 v[4:5], s[0:1], 0, v[130:131]
	s_mov_b32 s0, 0x6c400
	s_addc_u32 s17, s17, 0
	v_mul_lo_u32 v8, v3, s0
	v_lshl_add_u64 v[6:7], s[16:17], 0, v[130:131]
	v_mad_u32_u24 v8, v9, s33, v8
	v_lshlrev_b32_e32 v52, 6, v3
	v_lshlrev_b32_e32 v53, 2, v3
	v_lshl_add_u32 v54, v3, 14, v241
	v_lshl_add_u32 v55, v3, 3, v250
	s_mov_b64 s[16:17], 0
	v_readlane_b32 s19, v251, 22
	v_readlane_b32 s20, v251, 23
	v_readlane_b32 s21, v251, 24
	v_readlane_b32 s22, v251, 25
	v_readlane_b32 s23, v251, 26
	v_readlane_b32 s24, v251, 27
	v_readlane_b32 s25, v251, 28
	v_readlane_b32 s26, v251, 29
	v_readlane_b32 s27, v251, 30
	v_readlane_b32 s28, v251, 31
	v_readlane_b32 s29, v251, 32
	v_readlane_b32 s30, v251, 33
	v_readlane_b32 s31, v251, 34
	s_branch .LBB0_1409

.LBB0_1408:
	s_or_b64 exec, exec, s[18:19]
	s_movk_i32 s0, 0x234f
	v_add_u32_e32 v10, 0x600, v3
	v_cmp_lt_i32_e32 vcc, s0, v3
	v_add_u32_e32 v8, 0x28980000, v8
	v_add_u32_e32 v52, 0x18000, v52
	v_add_u32_e32 v53, 0x1800, v53
	v_add_u32_e32 v54, 0x1800000, v54
	v_add_u32_e32 v55, 0x3000, v55
	s_or_b64 s[16:17], vcc, s[16:17]
	v_mov_b32_e32 v3, v10
	s_andn2_b64 exec, exec, s[16:17]
	s_cbranch_execz .LBB0_1436
